# layers 1-3 LDS-index gather hand-rewritten: 4 rotating edge slots (8 row loads in flight per 16-lane group), fma_mix adds, exec-masked instead of clamped duplicate loads
# speedup vs baseline: 1.0495x; 1.0209x over previous
.LBB5_24:
	v_or_b32_e32 v46, 1, v35
	v_add_u32_e32 v46, s24, v46
	v_min_i32_e32 v46, 0x1869f, v46
	v_lshl_add_u32 v46, v46, 8, v26
	global_load_dwordx4 v[30:33], v46, s[4:5]
	s_mov_b64 s[22:23], exec
	s_movk_i32 s0, 0x2200
	v_sub_u32_e32 v27, v44, v28
	v_lshl_add_u32 v27, v27, 2, s0
	v_lshl_add_u32 v29, v44, 8, v26
	v_cmp_lt_i32_e64 s[2:3], v44, v45
	v_add_u32_e32 v46, 1, v44
	v_cmp_lt_i32_e64 s[16:17], v46, v45
	v_add_u32_e32 v46, 2, v44
	v_cmp_lt_i32_e64 s[18:19], v46, v45
	v_add_u32_e32 v46, 3, v44
	v_cmp_lt_i32_e64 s[20:21], v46, v45
	s_mov_b64 exec, s[2:3]
	ds_read_b32 v2, v27 offset:0
	global_load_dwordx4 v[4:7], v29, s[12:13] offset:0
	s_waitcnt lgkmcnt(0)
	v_lshl_add_u32 v2, v2, 8, v26
	global_load_dwordx4 v[8:11], v2, s[4:5]
	ds_read_b32 v2, v27 offset:16
	s_mov_b64 exec, s[16:17]
	ds_read_b32 v3, v27 offset:4
	global_load_dwordx4 v[12:15], v29, s[12:13] offset:256
	s_waitcnt lgkmcnt(0)
	v_lshl_add_u32 v3, v3, 8, v26
	global_load_dwordx4 v[16:19], v3, s[4:5]
	ds_read_b32 v3, v27 offset:20
	s_mov_b64 exec, s[18:19]
	ds_read_b32 v24, v27 offset:8
	global_load_dwordx4 v[20:23], v29, s[12:13] offset:512
	s_waitcnt lgkmcnt(0)
	v_lshl_add_u32 v24, v24, 8, v26
	global_load_dwordx4 v[50:53], v24, s[4:5]
	ds_read_b32 v24, v27 offset:24
	s_mov_b64 exec, s[20:21]
	ds_read_b32 v25, v27 offset:12
	global_load_dwordx4 v[54:57], v29, s[12:13] offset:768
	s_waitcnt lgkmcnt(0)
	v_lshl_add_u32 v25, v25, 8, v26
	global_load_dwordx4 v[58:61], v25, s[4:5]
	ds_read_b32 v25, v27 offset:28
	s_mov_b64 exec, s[22:23]
	s_cmp_eq_u64 s[2:3], 0
	s_cbranch_scc1 .Ll1_p1_empty
.Ll1_p1_loop:
	s_mov_b64 exec, s[2:3]
	s_waitcnt vmcnt(6)
	v_fma_mix_f32 v46, v8, 1.0, v4 op_sel_hi:[1,0,1]
	v_fma_mix_f32 v47, v8, 1.0, v4 op_sel:[1,0,1] op_sel_hi:[1,0,1]
	v_fma_mix_f32 v48, v9, 1.0, v5 op_sel_hi:[1,0,1]
	v_fma_mix_f32 v49, v9, 1.0, v5 op_sel:[1,0,1] op_sel_hi:[1,0,1]
	v_max_f32_e32 v46, 0, v46
	v_max_f32_e32 v47, 0, v47
	v_max_f32_e32 v48, 0, v48
	v_max_f32_e32 v49, 0, v49
	v_pk_add_f32 v[42:43], v[42:43], v[46:47]
	v_pk_add_f32 v[40:41], v[40:41], v[48:49]
	v_fma_mix_f32 v46, v10, 1.0, v6 op_sel_hi:[1,0,1]
	v_fma_mix_f32 v47, v10, 1.0, v6 op_sel:[1,0,1] op_sel_hi:[1,0,1]
	v_fma_mix_f32 v48, v11, 1.0, v7 op_sel_hi:[1,0,1]
	v_fma_mix_f32 v49, v11, 1.0, v7 op_sel:[1,0,1] op_sel_hi:[1,0,1]
	v_max_f32_e32 v46, 0, v46
	v_max_f32_e32 v47, 0, v47
	v_max_f32_e32 v48, 0, v48
	v_max_f32_e32 v49, 0, v49
	v_pk_add_f32 v[38:39], v[38:39], v[46:47]
	v_pk_add_f32 v[36:37], v[36:37], v[48:49]
	v_add_u32_e32 v46, 4, v44
	v_cmp_lt_i32_e64 s[2:3], v46, v45
	s_mov_b64 exec, s[2:3]
	global_load_dwordx4 v[4:7], v29, s[12:13] offset:1024
	s_waitcnt lgkmcnt(0)
	v_lshl_add_u32 v2, v2, 8, v26
	global_load_dwordx4 v[8:11], v2, s[4:5]
	ds_read_b32 v2, v27 offset:32
	s_mov_b64 exec, s[16:17]
	s_waitcnt vmcnt(6)
	v_fma_mix_f32 v46, v16, 1.0, v12 op_sel_hi:[1,0,1]
	v_fma_mix_f32 v47, v16, 1.0, v12 op_sel:[1,0,1] op_sel_hi:[1,0,1]
	v_fma_mix_f32 v48, v17, 1.0, v13 op_sel_hi:[1,0,1]
	v_fma_mix_f32 v49, v17, 1.0, v13 op_sel:[1,0,1] op_sel_hi:[1,0,1]
	v_max_f32_e32 v46, 0, v46
	v_max_f32_e32 v47, 0, v47
	v_max_f32_e32 v48, 0, v48
	v_max_f32_e32 v49, 0, v49
	v_pk_add_f32 v[42:43], v[42:43], v[46:47]
	v_pk_add_f32 v[40:41], v[40:41], v[48:49]
	v_fma_mix_f32 v46, v18, 1.0, v14 op_sel_hi:[1,0,1]
	v_fma_mix_f32 v47, v18, 1.0, v14 op_sel:[1,0,1] op_sel_hi:[1,0,1]
	v_fma_mix_f32 v48, v19, 1.0, v15 op_sel_hi:[1,0,1]
	v_fma_mix_f32 v49, v19, 1.0, v15 op_sel:[1,0,1] op_sel_hi:[1,0,1]
	v_max_f32_e32 v46, 0, v46
	v_max_f32_e32 v47, 0, v47
	v_max_f32_e32 v48, 0, v48
	v_max_f32_e32 v49, 0, v49
	v_pk_add_f32 v[38:39], v[38:39], v[46:47]
	v_pk_add_f32 v[36:37], v[36:37], v[48:49]
	v_add_u32_e32 v46, 5, v44
	v_cmp_lt_i32_e64 s[16:17], v46, v45
	s_mov_b64 exec, s[16:17]
	global_load_dwordx4 v[12:15], v29, s[12:13] offset:1280
	s_waitcnt lgkmcnt(0)
	v_lshl_add_u32 v3, v3, 8, v26
	global_load_dwordx4 v[16:19], v3, s[4:5]
	ds_read_b32 v3, v27 offset:36
	s_mov_b64 exec, s[18:19]
	s_waitcnt vmcnt(6)
	v_fma_mix_f32 v46, v50, 1.0, v20 op_sel_hi:[1,0,1]
	v_fma_mix_f32 v47, v50, 1.0, v20 op_sel:[1,0,1] op_sel_hi:[1,0,1]
	v_fma_mix_f32 v48, v51, 1.0, v21 op_sel_hi:[1,0,1]
	v_fma_mix_f32 v49, v51, 1.0, v21 op_sel:[1,0,1] op_sel_hi:[1,0,1]
	v_max_f32_e32 v46, 0, v46
	v_max_f32_e32 v47, 0, v47
	v_max_f32_e32 v48, 0, v48
	v_max_f32_e32 v49, 0, v49
	v_pk_add_f32 v[42:43], v[42:43], v[46:47]
	v_pk_add_f32 v[40:41], v[40:41], v[48:49]
	v_fma_mix_f32 v46, v52, 1.0, v22 op_sel_hi:[1,0,1]
	v_fma_mix_f32 v47, v52, 1.0, v22 op_sel:[1,0,1] op_sel_hi:[1,0,1]
	v_fma_mix_f32 v48, v53, 1.0, v23 op_sel_hi:[1,0,1]
	v_fma_mix_f32 v49, v53, 1.0, v23 op_sel:[1,0,1] op_sel_hi:[1,0,1]
	v_max_f32_e32 v46, 0, v46
	v_max_f32_e32 v47, 0, v47
	v_max_f32_e32 v48, 0, v48
	v_max_f32_e32 v49, 0, v49
	v_pk_add_f32 v[38:39], v[38:39], v[46:47]
	v_pk_add_f32 v[36:37], v[36:37], v[48:49]
	v_add_u32_e32 v46, 6, v44
	v_cmp_lt_i32_e64 s[18:19], v46, v45
	s_mov_b64 exec, s[18:19]
	global_load_dwordx4 v[20:23], v29, s[12:13] offset:1536
	s_waitcnt lgkmcnt(0)
	v_lshl_add_u32 v24, v24, 8, v26
	global_load_dwordx4 v[50:53], v24, s[4:5]
	ds_read_b32 v24, v27 offset:40
	s_mov_b64 exec, s[20:21]
	s_waitcnt vmcnt(6)
	v_fma_mix_f32 v46, v58, 1.0, v54 op_sel_hi:[1,0,1]
	v_fma_mix_f32 v47, v58, 1.0, v54 op_sel:[1,0,1] op_sel_hi:[1,0,1]
	v_fma_mix_f32 v48, v59, 1.0, v55 op_sel_hi:[1,0,1]
	v_fma_mix_f32 v49, v59, 1.0, v55 op_sel:[1,0,1] op_sel_hi:[1,0,1]
	v_max_f32_e32 v46, 0, v46
	v_max_f32_e32 v47, 0, v47
	v_max_f32_e32 v48, 0, v48
	v_max_f32_e32 v49, 0, v49
	v_pk_add_f32 v[42:43], v[42:43], v[46:47]
	v_pk_add_f32 v[40:41], v[40:41], v[48:49]
	v_fma_mix_f32 v46, v60, 1.0, v56 op_sel_hi:[1,0,1]
	v_fma_mix_f32 v47, v60, 1.0, v56 op_sel:[1,0,1] op_sel_hi:[1,0,1]
	v_fma_mix_f32 v48, v61, 1.0, v57 op_sel_hi:[1,0,1]
	v_fma_mix_f32 v49, v61, 1.0, v57 op_sel:[1,0,1] op_sel_hi:[1,0,1]
	v_max_f32_e32 v46, 0, v46
	v_max_f32_e32 v47, 0, v47
	v_max_f32_e32 v48, 0, v48
	v_max_f32_e32 v49, 0, v49
	v_pk_add_f32 v[38:39], v[38:39], v[46:47]
	v_pk_add_f32 v[36:37], v[36:37], v[48:49]
	v_add_u32_e32 v46, 7, v44
	v_cmp_lt_i32_e64 s[20:21], v46, v45
	s_mov_b64 exec, s[20:21]
	global_load_dwordx4 v[54:57], v29, s[12:13] offset:1792
	s_waitcnt lgkmcnt(0)
	v_lshl_add_u32 v25, v25, 8, v26
	global_load_dwordx4 v[58:61], v25, s[4:5]
	ds_read_b32 v25, v27 offset:44
	s_mov_b64 exec, s[22:23]
	v_add_u32_e32 v44, 4, v44
	v_add_u32_e32 v27, 16, v27
	v_add_u32_e32 v29, 0x400, v29
	s_cmp_lg_u64 s[2:3], 0
	s_cbranch_scc1 .Ll1_p1_loop
	s_branch .Ll1_p1_done

.Ll1_p1_done:
	s_movk_i32 s2, 0x110
	v_cvt_pk_f16_f32 v5, v36, v37
	v_cvt_pk_f16_f32 v4, v38, v39
	v_cvt_pk_f16_f32 v3, v40, v41
	v_cvt_pk_f16_f32 v2, v42, v43
	v_and_b32_e32 v46, 30, v35
	v_mad_u32_u24 v46, v46, s2, v26
	ds_write_b128 v46, v[2:5]
	v_or_b32_e32 v47, 1, v35
	v_mov_b32_e32 v46, 0x3200
	v_lshl_or_b32 v46, v47, 2, v46
	ds_read2_b32 v[44:45], v46 offset1:1
	v_add_u32_e32 v46, s24, v47
	s_mov_b32 s2, 0x186a0
	v_cmp_gt_i32_e32 vcc, s2, v46
	v_cvt_f32_f16_e32 v42, v30
	v_cvt_f32_f16_sdwa v43, v30 dst_sel:DWORD dst_unused:UNUSED_PAD src0_sel:WORD_1
	v_cvt_f32_f16_e32 v40, v31
	v_cvt_f32_f16_sdwa v41, v31 dst_sel:DWORD dst_unused:UNUSED_PAD src0_sel:WORD_1
	v_cvt_f32_f16_e32 v38, v32
	v_cvt_f32_f16_sdwa v39, v32 dst_sel:DWORD dst_unused:UNUSED_PAD src0_sel:WORD_1
	v_cvt_f32_f16_e32 v36, v33
	v_cvt_f32_f16_sdwa v37, v33 dst_sel:DWORD dst_unused:UNUSED_PAD src0_sel:WORD_1
	v_mul_f32_e32 v36, v34, v36
	v_mul_f32_e32 v37, v34, v37
	v_mul_f32_e32 v38, v34, v38
	v_mul_f32_e32 v39, v34, v39
	v_mul_f32_e32 v40, v34, v40
	v_mul_f32_e32 v41, v34, v41
	v_mul_f32_e32 v42, v34, v42
	v_mul_f32_e32 v43, v34, v43
	v_cndmask_b32_e32 v36, 0, v36, vcc
	v_cndmask_b32_e32 v37, 0, v37, vcc
	v_cndmask_b32_e32 v38, 0, v38, vcc
	v_cndmask_b32_e32 v39, 0, v39, vcc
	v_cndmask_b32_e32 v40, 0, v40, vcc
	v_cndmask_b32_e32 v41, 0, v41, vcc
	v_cndmask_b32_e32 v42, 0, v42, vcc
	v_cndmask_b32_e32 v43, 0, v43, vcc
	s_waitcnt lgkmcnt(0)
	v_sub_u32_e32 v27, v44, v28
	v_lshl_add_u32 v27, v27, 2, s0
	v_lshl_add_u32 v29, v44, 8, v26
	v_cmp_lt_i32_e64 s[2:3], v44, v45
	v_add_u32_e32 v46, 1, v44
	v_cmp_lt_i32_e64 s[16:17], v46, v45
	v_add_u32_e32 v46, 2, v44
	v_cmp_lt_i32_e64 s[18:19], v46, v45
	v_add_u32_e32 v46, 3, v44
	v_cmp_lt_i32_e64 s[20:21], v46, v45
	s_mov_b64 exec, s[2:3]
	ds_read_b32 v2, v27 offset:0
	global_load_dwordx4 v[4:7], v29, s[12:13] offset:0
	s_waitcnt lgkmcnt(0)
	v_lshl_add_u32 v2, v2, 8, v26
	global_load_dwordx4 v[8:11], v2, s[4:5]
	ds_read_b32 v2, v27 offset:16
	s_mov_b64 exec, s[16:17]
	ds_read_b32 v3, v27 offset:4
	global_load_dwordx4 v[12:15], v29, s[12:13] offset:256
	s_waitcnt lgkmcnt(0)
	v_lshl_add_u32 v3, v3, 8, v26
	global_load_dwordx4 v[16:19], v3, s[4:5]
	ds_read_b32 v3, v27 offset:20
	s_mov_b64 exec, s[18:19]
	ds_read_b32 v24, v27 offset:8
	global_load_dwordx4 v[20:23], v29, s[12:13] offset:512
	s_waitcnt lgkmcnt(0)
	v_lshl_add_u32 v24, v24, 8, v26
	global_load_dwordx4 v[50:53], v24, s[4:5]
	ds_read_b32 v24, v27 offset:24
	s_mov_b64 exec, s[20:21]
	ds_read_b32 v25, v27 offset:12
	global_load_dwordx4 v[54:57], v29, s[12:13] offset:768
	s_waitcnt lgkmcnt(0)
	v_lshl_add_u32 v25, v25, 8, v26
	global_load_dwordx4 v[58:61], v25, s[4:5]
	ds_read_b32 v25, v27 offset:28
	s_mov_b64 exec, s[22:23]
	s_cmp_eq_u64 s[2:3], 0
	s_cbranch_scc1 .Ll1_p2_empty

.Ll1_p2_done:
	v_or_b32_e32 v27, 1, v35
	v_mov_b32_e32 v34, v42
	v_mov_b32_e32 v35, v43
	v_mov_b32_e32 v46, v40
	v_mov_b32_e32 v47, v41
	v_mov_b32_e32 v48, v38
	v_mov_b32_e32 v49, v39
	v_mov_b32_e32 v50, v36
	v_mov_b32_e32 v51, v37
	s_branch .LBB5_61

.LBB5_37:
	s_or_b64 exec, exec, s[2:3]
	s_waitcnt lgkmcnt(0)
	v_cmp_lt_i32_e64 s[0:1], v40, v41
	v_mov_b32_e32 v51, v37
	v_mov_b32_e32 v50, v36
	v_mov_b32_e32 v49, v39
	v_mov_b32_e32 v48, v38
	v_mov_b32_e32 v47, v43
	v_mov_b32_e32 v46, v42
	v_mov_b32_e32 v35, v45
	v_mov_b32_e32 v34, v44
	s_and_saveexec_b64 s[4:5], s[0:1]
	s_cbranch_execz .LBB5_49
	v_ashrrev_i32_e32 v3, 31, v40
	v_mov_b32_e32 v2, v40
	v_lshl_add_u64 v[4:5], v[2:3], 2, s[14:15]
	v_lshlrev_b64 v[2:3], 8, v[2:3]
	v_lshl_or_b32 v2, v1, 4, v2
	v_lshl_add_u64 v[52:53], v[4:5], 0, 4
	v_lshl_add_u64 v[54:55], s[12:13], 0, v[2:3]
	s_mov_b64 s[16:17], 0
	s_mov_b64 s[18:19], 0x400
	v_mov_b32_e32 v29, v40
	v_mov_b64_e32 v[34:35], v[44:45]
	v_mov_b64_e32 v[46:47], v[42:43]
	v_mov_b64_e32 v[48:49], v[38:39]
	v_mov_b64_e32 v[50:51], v[36:37]
	s_branch .LBB5_41

.LBB5_46:
	v_cvt_f32_f16_e32 v10, v2
	v_cvt_f32_f16_e32 v11, v6
	v_cvt_f32_f16_sdwa v2, v2 dst_sel:DWORD dst_unused:UNUSED_PAD src0_sel:WORD_1
	v_cvt_f32_f16_sdwa v6, v6 dst_sel:DWORD dst_unused:UNUSED_PAD src0_sel:WORD_1
	v_add_f32_e32 v10, v10, v11
	v_max_f32_e32 v10, 0, v10
	v_add_f32_e32 v2, v2, v6
	v_max_f32_e32 v11, 0, v2
	v_cvt_f32_f16_e32 v2, v3
	v_cvt_f32_f16_e32 v6, v7
	v_cvt_f32_f16_sdwa v3, v3 dst_sel:DWORD dst_unused:UNUSED_PAD src0_sel:WORD_1
	v_cvt_f32_f16_sdwa v7, v7 dst_sel:DWORD dst_unused:UNUSED_PAD src0_sel:WORD_1
	v_pk_add_f32 v[34:35], v[10:11], v[34:35]
	v_add_f32_e32 v2, v2, v6
	v_cvt_f32_f16_e32 v6, v4
	v_add_f32_e32 v3, v3, v7
	v_cvt_f32_f16_e32 v7, v8
	v_cvt_f32_f16_sdwa v4, v4 dst_sel:DWORD dst_unused:UNUSED_PAD src0_sel:WORD_1
	v_cvt_f32_f16_sdwa v8, v8 dst_sel:DWORD dst_unused:UNUSED_PAD src0_sel:WORD_1
	v_max_f32_e32 v2, 0, v2
	v_max_f32_e32 v3, 0, v3
	v_pk_add_f32 v[46:47], v[2:3], v[46:47]
	v_add_f32_e32 v2, v6, v7
	v_add_f32_e32 v3, v4, v8
	v_cvt_f32_f16_e32 v4, v5
	v_cvt_f32_f16_e32 v6, v9
	v_cvt_f32_f16_sdwa v5, v5 dst_sel:DWORD dst_unused:UNUSED_PAD src0_sel:WORD_1
	v_cvt_f32_f16_sdwa v7, v9 dst_sel:DWORD dst_unused:UNUSED_PAD src0_sel:WORD_1
	v_max_f32_e32 v2, 0, v2
	v_max_f32_e32 v3, 0, v3
	v_pk_add_f32 v[48:49], v[2:3], v[48:49]
	v_add_f32_e32 v2, v4, v6
	v_add_f32_e32 v3, v5, v7
	v_max_f32_e32 v2, 0, v2
	v_max_f32_e32 v3, 0, v3
	v_pk_add_f32 v[50:51], v[2:3], v[50:51]
	s_branch .LBB5_40
.LBB5_48:
	s_or_b64 exec, exec, s[16:17]
.LBB5_49:
	s_or_b64 exec, exec, s[4:5]
.LBB5_61:
	v_and_b32_e32 v21, 63, v0
	v_lshrrev_b32_e32 v20, 5, v0
	v_and_b32_e32 v19, 6, v20
	s_waitcnt vmcnt(2)
	v_lshlrev_b32_e32 v2, 4, v21
	v_or_b32_e32 v18, 1, v20
	s_waitcnt vmcnt(1)
	v_lshl_or_b32 v14, v19, 10, v2
	v_lshl_or_b32 v2, v18, 10, v2
	global_load_dwordx4 v[22:25], v14, s[10:11]
	global_load_dwordx4 v[28:31], v2, s[10:11]
	v_or_b32_e32 v2, 0x2000, v14
	global_load_dwordx4 v[36:39], v2, s[10:11]
	v_or_b32_e32 v2, 0x2400, v14
	global_load_dwordx4 v[40:43], v2, s[10:11]
	v_or_b32_e32 v2, 0x4000, v14
	global_load_dwordx4 v[10:13], v2, s[10:11]
	v_or_b32_e32 v2, 0x4400, v14
	global_load_dwordx4 v[6:9], v2, s[10:11]
	v_or_b32_e32 v2, 0x6000, v14
	global_load_dwordx4 v[2:5], v2, s[10:11]
	v_or_b32_e32 v14, 0x6400, v14
	global_load_dwordx4 v[14:17], v14, s[10:11]
	s_movk_i32 s0, 0x110
	v_and_b32_e32 v32, 48, v0
	v_cvt_pk_f16_f32 v51, v50, v51
	v_cvt_pk_f16_f32 v50, v48, v49
	v_cvt_pk_f16_f32 v49, v46, v47
	v_cvt_pk_f16_f32 v48, v34, v35
	v_mad_u32_u24 v27, v27, s0, v26
	v_mad_u32_u24 v60, v1, s0, v32
	ds_write_b128 v27, v[48:51]
	s_waitcnt lgkmcnt(0)
	s_barrier
	ds_read_b128 v[32:35], v60
	ds_read_b128 v[44:47], v60 offset:64
	ds_read_b128 v[52:55], v60 offset:4352
	ds_read_b128 v[56:59], v60 offset:4416
	v_mbcnt_lo_u32_b32 v27, -1, 0
	v_mbcnt_hi_u32_b32 v27, -1, v27
	s_ashr_i32 s0, s25, 31
	s_lshr_b32 s0, s0, 29
	s_add_i32 s0, s25, s0
	s_and_b32 s0, s0, 0xfffff8
	s_sub_i32 s0, s25, s0
	s_lshl_b32 s0, s0, 8
	s_ashr_i32 s1, s0, 31
	s_lshl_b64 s[0:1], s[0:1], 2
	s_add_u32 s0, s8, s0
	s_addc_u32 s1, s9, s1
	s_waitcnt vmcnt(7) lgkmcnt(3)
	v_mfma_f32_16x16x32_f16 v[48:51], v[32:35], v[22:25], 0
	s_waitcnt vmcnt(6)
	v_mfma_f32_16x16x32_f16 v[32:35], v[32:35], v[28:31], 0
	s_waitcnt lgkmcnt(1)
	v_mfma_f32_16x16x32_f16 v[22:25], v[52:55], v[22:25], 0
	v_mfma_f32_16x16x32_f16 v[28:31], v[52:55], v[28:31], 0
	s_waitcnt vmcnt(5)
	v_mfma_f32_16x16x32_f16 v[48:51], v[44:47], v[36:39], v[48:51]
	s_waitcnt vmcnt(4)
	v_mfma_f32_16x16x32_f16 v[32:35], v[44:47], v[40:43], v[32:35]
	s_waitcnt lgkmcnt(0)
	v_mfma_f32_16x16x32_f16 v[22:25], v[56:59], v[36:39], v[22:25]
	v_mfma_f32_16x16x32_f16 v[28:31], v[56:59], v[40:43], v[28:31]
	ds_read_b128 v[36:39], v60 offset:128
	ds_read_b128 v[40:43], v60 offset:4480
	ds_read_b128 v[44:47], v60 offset:192
	s_waitcnt vmcnt(3) lgkmcnt(2)
	v_mfma_f32_16x16x32_f16 v[48:51], v[36:39], v[10:13], v[48:51]
	s_waitcnt vmcnt(2)
	v_mfma_f32_16x16x32_f16 v[32:35], v[36:39], v[6:9], v[32:35]
	ds_read_b128 v[36:39], v60 offset:4544
	s_waitcnt lgkmcnt(2)
	v_mfma_f32_16x16x32_f16 v[52:55], v[40:43], v[10:13], v[22:25]
	v_and_b32_e32 v10, 64, v27
	s_nop 1
	v_xor_b32_e32 v22, 16, v27
	v_mfma_f32_16x16x32_f16 v[28:31], v[40:43], v[6:9], v[28:31]
	v_add_u32_e32 v6, 64, v10
	v_xor_b32_e32 v23, 32, v27
	v_cmp_lt_i32_e32 vcc, v22, v6
	s_waitcnt vmcnt(1) lgkmcnt(1)
	v_mfma_f32_16x16x32_f16 v[10:13], v[44:47], v[2:5], v[48:51]
	v_cndmask_b32_e32 v22, v27, v22, vcc
	v_cmp_lt_i32_e32 vcc, v23, v6
	s_waitcnt lgkmcnt(0)
	v_mfma_f32_16x16x32_f16 v[2:5], v[36:39], v[2:5], v[52:55]
	v_cndmask_b32_e32 v24, v27, v23, vcc
	v_lshlrev_b32_e32 v23, 2, v22
	v_lshlrev_b32_e32 v22, 2, v24
	s_nop 0
	v_add_f32_e32 v24, 0, v10
	v_mul_f32_e32 v25, v11, v11
	v_add_f32_e32 v24, v24, v11
	v_fmac_f32_e32 v25, v10, v10
	v_add_f32_e32 v24, v24, v12
	v_fmac_f32_e32 v25, v12, v12
	v_add_f32_e32 v24, v24, v13
	v_fmac_f32_e32 v25, v13, v13
	v_add_f32_e32 v24, v24, v2
	v_fmac_f32_e32 v25, v2, v2
	v_add_f32_e32 v24, v24, v3
	v_fmac_f32_e32 v25, v3, v3
	v_add_f32_e32 v24, v24, v4
	v_fmac_f32_e32 v25, v4, v4
	v_add_f32_e32 v24, v24, v5
	v_fmac_f32_e32 v25, v5, v5
	s_waitcnt vmcnt(0)
	v_mfma_f32_16x16x32_f16 v[6:9], v[44:47], v[14:17], v[32:35]
	ds_bpermute_b32 v27, v23, v24
	v_cmp_gt_u32_e32 vcc, 16, v21
	v_lshlrev_b32_e32 v21, 2, v1
	ds_bpermute_b32 v32, v23, v25
	v_mfma_f32_16x16x32_f16 v[14:17], v[36:39], v[14:17], v[28:31]
	s_waitcnt lgkmcnt(1)
	v_add_f32_e32 v24, v24, v27
	ds_bpermute_b32 v27, v22, v24
	s_waitcnt lgkmcnt(1)
	v_add_f32_e32 v25, v25, v32
	ds_bpermute_b32 v28, v22, v25
	s_and_saveexec_b64 s[2:3], vcc
	s_cbranch_execz .LBB5_63
	s_waitcnt lgkmcnt(1)
	v_add_f32_e32 v24, v24, v27
	v_lshl_or_b32 v27, v19, 6, v21
	s_waitcnt lgkmcnt(0)
	v_add_f32_e32 v25, v25, v28
	global_atomic_add_f32 v27, v24, s[0:1]
	global_atomic_add_f32 v27, v25, s[0:1] offset:512
